# speedup vs baseline: 1.0066x; 1.0013x over previous
.LBB2_14:
	s_or_b64 exec, exec, s[6:7]
	v_and_b32_e32 v147, 15, v0
	v_and_b32_e32 v1, 48, v0
	s_movk_i32 s2, 0x150
	v_mad_u32_u24 v1, v147, s2, v1
	s_waitcnt lgkmcnt(0)
	s_barrier
	ds_read_b128 v[130:133], v1
	ds_read_b128 v[122:125], v1 offset:64
	ds_read_b128 v[118:121], v1 offset:128
	ds_read_b128 v[110:113], v1 offset:192
	ds_read_b128 v[102:105], v1 offset:256
	ds_read_b128 v[86:89], v1 offset:5376
	ds_read_b128 v[90:93], v1 offset:5440
	ds_read_b128 v[94:97], v1 offset:5504
	ds_read_b128 v[98:101], v1 offset:5568
	ds_read_b128 v[82:85], v1 offset:5632
	ds_read_b128 v[66:69], v1 offset:10752
	ds_read_b128 v[70:73], v1 offset:10816
	ds_read_b128 v[74:77], v1 offset:10880
	ds_read_b128 v[78:81], v1 offset:10944
	ds_read_b128 v[62:65], v1 offset:11008
	ds_read_b128 v[46:49], v1 offset:16128
	ds_read_b128 v[50:53], v1 offset:16192
	ds_read_b128 v[54:57], v1 offset:16256
	ds_read_b128 v[58:61], v1 offset:16320
	ds_read_b128 v[42:45], v1 offset:16384
	s_waitcnt lgkmcnt(0)
	s_barrier
	s_andn2_b64 vcc, exec, s[4:5]
	s_cbranch_vccnz .LBB2_26
	v_mov_b32_e32 v148, 0x9480
	v_lshl_add_u32 v148, v0, 4, v148
	v_mov_b32_e32 v142, 0
	v_mov_b32_e32 v143, 0
	v_mov_b32_e32 v144, 0
	v_mov_b32_e32 v145, 0
	s_movk_i32 s2, 0x108
	v_cmp_gt_u32_e32 vcc, s2, v0
	s_and_saveexec_b64 s[2:3], vcc
	ds_write_b128 v148, v[142:145]
	s_nop 1
	s_or_b64 exec, exec, s[2:3]
